# baseline (speedup 1.0000x reference)
.LBB5_6:
	s_or_b64 exec, exec, s[16:17]
	v_mov_b32_e32 v29, 0
	v_and_b32_e32 v0, 15, v0
	v_lshrrev_b32_e32 v27, 4, v71
	s_waitcnt lgkmcnt(0)
	v_lshl_add_u64 v[84:85], s[8:9], 0, v[28:29]
	v_lshlrev_b32_e32 v28, 4, v71
	v_cmp_gt_u32_e32 vcc, 10, v0
	v_lshlrev_b32_e32 v0, 4, v0
	v_and_or_b32 v26, v26, 60, v27
	v_lshl_add_u64 v[88:89], s[10:11], 0, v[28:29]
	v_lshlrev_b32_e32 v28, 1, v0
	v_and_b32_e32 v0, 12, v94
	v_lshlrev_b32_e32 v70, 3, v70
	v_lshlrev_b32_e32 v95, 2, v26
	v_lshl_add_u64 v[26:27], s[6:7], 0, v[28:29]
	v_lshlrev_b32_e32 v28, 1, v0
	v_lshl_add_u64 v[86:87], v[26:27], 0, v[28:29]
	v_lshlrev_b32_e32 v96, 2, v70
	s_barrier
	s_and_saveexec_b64 s[0:1], s[2:3]
	s_cbranch_execz .LBB5_9
	v_lshlrev_b32_e32 v0, 4, v1
	ds_read_b128 v[70:73], v96
	ds_read_b128 v[74:77], v96 offset:512
	v_or_b32_e32 v90, v0, v94
	v_ashrrev_i32_e32 v91, 31, v90
	v_lshlrev_b64 v[26:27], 8, v[90:91]
	v_lshl_add_u64 v[92:93], v[82:83], 0, v[26:27]
	global_load_dwordx4 v[112:115], v[88:89], off
	global_load_dwordx4 v[116:119], v[88:89], off offset:1024
	global_load_dwordx4 v[120:123], v[88:89], off offset:2048
	global_load_dwordx4 v[124:127], v[88:89], off offset:3072
	s_waitcnt vmcnt(0)
	s_and_saveexec_b64 s[20:21], s[4:5]
	s_cbranch_execz .LBB5_4
	v_lshl_or_b32 v2, v97, 4, v94
	v_ashrrev_i32_e32 v3, 31, v2
	v_lshlrev_b64 v[2:3], 8, v[2:3]
	v_lshl_add_u64 v[4:5], v[4:5], 0, v[2:3]
	v_lshl_add_u64 v[6:7], v[82:83], 0, v[2:3]
	global_load_dwordx4 v[38:41], v[4:5], off
	global_load_dwordx4 v[18:21], v[4:5], off offset:64
	global_load_dwordx4 v[42:45], v[6:7], off
	global_load_dwordx4 v[22:25], v[6:7], off offset:64
	global_load_dwordx4 v[10:13], v[4:5], off offset:128
	s_nop 0
	global_load_dwordx4 v[2:5], v[4:5], off offset:192
	s_nop 0
	global_load_dwordx4 v[14:17], v[6:7], off offset:128
	s_nop 0
	global_load_dwordx4 v[6:9], v[6:7], off offset:192
.LBB5_4:
	s_or_b64 exec, exec, s[20:21]
	v_cvt_f32_f16_sdwa v27, v66 dst_sel:DWORD dst_unused:UNUSED_PAD src0_sel:WORD_1
	v_cvt_f32_f16_e32 v26, v66
	s_waitcnt lgkmcnt(0)
	v_fma_mix_f32 v1, v70, v62, v74 op_sel_hi:[0,1,0]
	v_max_f32_e32 v70, 0, v1
	v_fma_mix_f32 v1, v71, v62, v75 op_sel:[0,1,0] op_sel_hi:[0,1,0]
	v_max_f32_e32 v71, 0, v1
	ds_read_b128 v[78:81], v96 offset:16
	ds_read_b128 v[98:101], v96 offset:528
	v_pk_add_f32 v[26:27], v[70:71], v[26:27]
	v_cvt_f32_f16_sdwa v71, v67 dst_sel:DWORD dst_unused:UNUSED_PAD src0_sel:WORD_1
	v_cvt_f32_f16_e32 v70, v67
	v_fma_mix_f32 v1, v72, v63, v76 op_sel_hi:[0,1,0]
	v_max_f32_e32 v62, 0, v1
	v_fma_mix_f32 v1, v73, v63, v77 op_sel:[0,1,0] op_sel_hi:[0,1,0]
	v_max_f32_e32 v63, 0, v1
	v_pk_add_f32 v[70:71], v[62:63], v[70:71]
	v_cvt_f32_f16_sdwa v63, v68 dst_sel:DWORD dst_unused:UNUSED_PAD src0_sel:WORD_1
	v_cvt_f32_f16_e32 v62, v68
	s_waitcnt lgkmcnt(0)
	v_fma_mix_f32 v1, v78, v64, v98 op_sel_hi:[0,1,0]
	v_max_f32_e32 v72, 0, v1
	v_fma_mix_f32 v1, v79, v64, v99 op_sel:[0,1,0] op_sel_hi:[0,1,0]
	v_cvt_f32_f16_sdwa v75, v69 dst_sel:DWORD dst_unused:UNUSED_PAD src0_sel:WORD_1
	v_cvt_f32_f16_e32 v74, v69
	v_max_f32_e32 v73, 0, v1
	v_fma_mix_f32 v1, v80, v65, v100 op_sel_hi:[0,1,0]
	v_pk_add_f32 v[72:73], v[72:73], v[62:63]
	v_max_f32_e32 v64, 0, v1
	v_fma_mix_f32 v1, v81, v65, v101 op_sel:[0,1,0] op_sel_hi:[0,1,0]
	v_mov_b32_e32 v62, v29
	v_max_f32_e32 v65, 0, v1
	v_cvt_pk_fp8_f32 v62, v26, v27
	v_cvt_pk_f16_f32 v66, v26, v27
	v_pk_add_f32 v[26:27], v[64:65], v[74:75]
	v_cvt_pk_f16_f32 v67, v70, v71
	v_cvt_pk_f16_f32 v68, v72, v73
	v_cvt_pk_f16_f32 v69, v26, v27
	v_mov_b32_e32 v63, v29
	global_store_dwordx4 v[92:93], v[66:69], off
	v_cvt_pk_fp8_f32 v63, v72, v73
	v_cvt_pk_fp8_f32 v62, v70, v71 op_sel:[0,0,1]
	ds_read_b128 v[70:73], v96 offset:128
	ds_read_b128 v[74:77], v96 offset:640
	ds_read_b128 v[78:81], v96 offset:144
	ds_read_b128 v[98:101], v96 offset:656
	v_cvt_pk_fp8_f32 v63, v26, v27 op_sel:[0,0,1]
	s_nop 0
	v_cvt_f32_f16_sdwa v27, v58 dst_sel:DWORD dst_unused:UNUSED_PAD src0_sel:WORD_1
	v_cvt_f32_f16_e32 v26, v58
	s_waitcnt lgkmcnt(2)
	v_fma_mix_f32 v1, v70, v54, v74 op_sel_hi:[0,1,0]
	v_max_f32_e32 v64, 0, v1
	v_fma_mix_f32 v1, v71, v54, v75 op_sel:[0,1,0] op_sel_hi:[0,1,0]
	v_max_f32_e32 v65, 0, v1
	v_pk_add_f32 v[26:27], v[64:65], v[26:27]
	v_cvt_f32_f16_sdwa v65, v59 dst_sel:DWORD dst_unused:UNUSED_PAD src0_sel:WORD_1
	v_cvt_f32_f16_e32 v64, v59
	v_fma_mix_f32 v1, v72, v55, v76 op_sel_hi:[0,1,0]
	v_max_f32_e32 v58, 0, v1
	v_fma_mix_f32 v1, v73, v55, v77 op_sel:[0,1,0] op_sel_hi:[0,1,0]
	v_max_f32_e32 v59, 0, v1
	v_pk_add_f32 v[58:59], v[58:59], v[64:65]
	v_cvt_f32_f16_sdwa v65, v60 dst_sel:DWORD dst_unused:UNUSED_PAD src0_sel:WORD_1
	v_cvt_f32_f16_e32 v64, v60
	s_waitcnt lgkmcnt(0)
	v_fma_mix_f32 v1, v78, v56, v98 op_sel_hi:[0,1,0]
	v_max_f32_e32 v70, 0, v1
	v_fma_mix_f32 v1, v79, v56, v99 op_sel:[0,1,0] op_sel_hi:[0,1,0]
	v_cvt_f32_f16_sdwa v75, v61 dst_sel:DWORD dst_unused:UNUSED_PAD src0_sel:WORD_1
	v_cvt_f32_f16_e32 v74, v61
	v_max_f32_e32 v71, 0, v1
	v_fma_mix_f32 v1, v80, v57, v100 op_sel_hi:[0,1,0]
	v_pk_add_f32 v[70:71], v[70:71], v[64:65]
	v_max_f32_e32 v72, 0, v1
	v_fma_mix_f32 v1, v81, v57, v101 op_sel:[0,1,0] op_sel_hi:[0,1,0]
	v_mov_b32_e32 v64, v29
	v_max_f32_e32 v73, 0, v1
	v_cvt_pk_fp8_f32 v64, v26, v27
	v_cvt_pk_f16_f32 v54, v26, v27
	v_pk_add_f32 v[26:27], v[72:73], v[74:75]
	v_cvt_pk_f16_f32 v55, v58, v59
	v_cvt_pk_f16_f32 v56, v70, v71
	v_cvt_pk_f16_f32 v57, v26, v27
	v_mov_b32_e32 v65, v29
	global_store_dwordx4 v[92:93], v[54:57], off offset:64
	v_cvt_pk_fp8_f32 v65, v70, v71
	v_cvt_pk_fp8_f32 v64, v58, v59 op_sel:[0,0,1]
	ds_read_b128 v[58:61], v96 offset:256
	ds_read_b128 v[70:73], v96 offset:768
	ds_read_b128 v[74:77], v96 offset:272
	ds_read_b128 v[78:81], v96 offset:784
	v_cvt_pk_fp8_f32 v65, v26, v27 op_sel:[0,0,1]
	s_nop 0
	v_cvt_f32_f16_sdwa v27, v50 dst_sel:DWORD dst_unused:UNUSED_PAD src0_sel:WORD_1
	v_cvt_f32_f16_e32 v26, v50
	s_waitcnt lgkmcnt(2)
	v_fma_mix_f32 v1, v58, v46, v70 op_sel_hi:[0,1,0]
	v_max_f32_e32 v58, 0, v1
	v_fma_mix_f32 v1, v59, v46, v71 op_sel:[0,1,0] op_sel_hi:[0,1,0]
	v_max_f32_e32 v59, 0, v1
	v_fma_mix_f32 v1, v60, v47, v72 op_sel_hi:[0,1,0]
	v_pk_add_f32 v[58:59], v[58:59], v[26:27]
	v_max_f32_e32 v26, 0, v1
	v_cvt_f32_f16_sdwa v107, v51 dst_sel:DWORD dst_unused:UNUSED_PAD src0_sel:WORD_1
	v_cvt_f32_f16_e32 v106, v51
	v_fma_mix_f32 v1, v61, v47, v73 op_sel:[0,1,0] op_sel_hi:[0,1,0]
	v_max_f32_e32 v27, 0, v1
	v_pk_add_f32 v[50:51], v[26:27], v[106:107]
	s_waitcnt lgkmcnt(0)
	v_fma_mix_f32 v1, v74, v48, v78 op_sel_hi:[0,1,0]
	v_cvt_f32_f16_sdwa v27, v52 dst_sel:DWORD dst_unused:UNUSED_PAD src0_sel:WORD_1
	v_cvt_f32_f16_e32 v26, v52
	v_max_f32_e32 v60, 0, v1
	v_fma_mix_f32 v1, v75, v48, v79 op_sel:[0,1,0] op_sel_hi:[0,1,0]
	v_max_f32_e32 v61, 0, v1
	v_fma_mix_f32 v1, v76, v49, v80 op_sel_hi:[0,1,0]
	v_max_f32_e32 v74, 0, v1
	v_fma_mix_f32 v1, v77, v49, v81 op_sel:[0,1,0] op_sel_hi:[0,1,0]
	v_cvt_f32_f16_sdwa v77, v53 dst_sel:DWORD dst_unused:UNUSED_PAD src0_sel:WORD_1
	v_cvt_f32_f16_e32 v76, v53
	v_pk_add_f32 v[60:61], v[60:61], v[26:27]
	v_mov_b32_e32 v26, v29
	v_mov_b32_e32 v27, v29
	v_max_f32_e32 v75, 0, v1
	v_cvt_pk_fp8_f32 v26, v58, v59
	v_cvt_pk_fp8_f32 v27, v60, v61
	v_pk_add_f32 v[52:53], v[74:75], v[76:77]
	v_cvt_pk_f16_f32 v46, v58, v59
	v_cvt_pk_f16_f32 v47, v50, v51
	v_cvt_pk_f16_f32 v48, v60, v61
	v_cvt_pk_f16_f32 v49, v52, v53
	global_store_dwordx4 v[92:93], v[46:49], off offset:128
	v_cvt_pk_fp8_f32 v26, v50, v51 op_sel:[0,0,1]
	v_cvt_pk_fp8_f32 v27, v52, v53 op_sel:[0,0,1]
	ds_read_b128 v[50:53], v96 offset:384
	ds_read_b128 v[58:61], v96 offset:896
	ds_read_b128 v[74:77], v96 offset:400
	ds_read_b128 v[78:81], v96 offset:912
	ds_bpermute_b32 v66, v95, v66
	ds_bpermute_b32 v67, v95, v67
	ds_bpermute_b32 v68, v95, v68
	s_waitcnt lgkmcnt(5)
	v_fma_mix_f32 v1, v50, v30, v58 op_sel_hi:[0,1,0]
	ds_bpermute_b32 v69, v95, v69
	v_max_f32_e32 v50, 0, v1
	v_fma_mix_f32 v1, v51, v30, v59 op_sel:[0,1,0] op_sel_hi:[0,1,0]
	s_nop 0
	v_cvt_f32_f16_sdwa v59, v35 dst_sel:DWORD dst_unused:UNUSED_PAD src0_sel:WORD_1
	v_cvt_f32_f16_e32 v58, v35
	v_max_f32_e32 v51, 0, v1
	v_fma_mix_f32 v1, v52, v31, v60 op_sel_hi:[0,1,0]
	v_cvt_f32_f16_sdwa v111, v34 dst_sel:DWORD dst_unused:UNUSED_PAD src0_sel:WORD_1
	v_cvt_f32_f16_e32 v110, v34
	v_max_f32_e32 v34, 0, v1
	v_fma_mix_f32 v1, v53, v31, v61 op_sel:[0,1,0] op_sel_hi:[0,1,0]
	v_cvt_f32_f16_sdwa v53, v36 dst_sel:DWORD dst_unused:UNUSED_PAD src0_sel:WORD_1
	v_cvt_f32_f16_e32 v52, v36
	v_max_f32_e32 v35, 0, v1
	s_waitcnt lgkmcnt(4)
	v_fma_mix_f32 v1, v74, v32, v78 op_sel_hi:[0,1,0]
	ds_bpermute_b32 v54, v95, v54
	ds_bpermute_b32 v55, v95, v55
	ds_bpermute_b32 v56, v95, v56
	ds_bpermute_b32 v57, v95, v57
	v_pk_add_f32 v[34:35], v[34:35], v[58:59]
	v_max_f32_e32 v58, 0, v1
	v_fma_mix_f32 v1, v75, v32, v79 op_sel:[0,1,0] op_sel_hi:[0,1,0]
	v_max_f32_e32 v59, 0, v1
	v_pk_add_f32 v[52:53], v[58:59], v[52:53]
	v_cvt_f32_f16_sdwa v59, v37 dst_sel:DWORD dst_unused:UNUSED_PAD src0_sel:WORD_1
	v_cvt_f32_f16_e32 v58, v37
	v_pk_add_f32 v[50:51], v[50:51], v[110:111]
	v_fma_mix_f32 v1, v76, v33, v80 op_sel_hi:[0,1,0]
	v_mov_b32_e32 v28, v29
	ds_bpermute_b32 v46, v95, v46
	ds_bpermute_b32 v47, v95, v47
	ds_bpermute_b32 v48, v95, v48
	ds_bpermute_b32 v49, v95, v49
	v_max_f32_e32 v36, 0, v1
	v_fma_mix_f32 v1, v77, v33, v81 op_sel:[0,1,0] op_sel_hi:[0,1,0]
	v_cvt_pk_fp8_f32 v28, v50, v51
	v_cvt_pk_f16_f32 v30, v50, v51
	v_cvt_pk_f16_f32 v32, v52, v53
	v_max_f32_e32 v37, 0, v1
	v_cvt_pk_fp8_f32 v29, v52, v53
	s_waitcnt lgkmcnt(8)
	v_mfma_f32_16x16x32_f16 v[50:53], v[66:69], v[112:115], 0
	v_add_f32_e64 v58, v36, v58
	v_add_f32_e64 v59, v37, v59
	v_cvt_pk_f16_f32 v31, v34, v35
	v_cvt_pk_f16_f32 v33, v58, v59
	v_cvt_pk_fp8_f32 v28, v34, v35 op_sel:[0,0,1]
	ds_bpermute_b32 v34, v95, v30
	ds_bpermute_b32 v35, v95, v31
	ds_bpermute_b32 v36, v95, v32
	ds_bpermute_b32 v37, v95, v33
	s_waitcnt lgkmcnt(8)
	v_mfma_f32_16x16x32_f16 v[50:53], v[54:57], v[116:119], v[50:53]
	global_store_dwordx4 v[92:93], v[30:33], off offset:192
	v_cvt_pk_fp8_f32 v29, v58, v59 op_sel:[0,0,1]
	v_lshlrev_b64 v[54:55], 7, v[90:91]
	s_waitcnt lgkmcnt(4)
	v_mfma_f32_16x16x32_f16 v[30:33], v[46:49], v[120:123], v[50:53]
	v_lshl_add_u64 v[46:47], v[84:85], 0, v[54:55]
	global_store_dwordx4 v[46:47], v[62:65], off
	global_store_dwordx4 v[46:47], v[26:29], off offset:64
	s_waitcnt lgkmcnt(0)
	s_nop 0
	v_mfma_f32_16x16x32_f16 v[26:29], v[34:37], v[124:127], v[30:33]
	s_and_b64 exec, exec, vcc
	s_cbranch_execz .LBB5_9
	v_mul_u32_u24_e32 v0, 10, v0
	v_ashrrev_i32_e32 v1, 31, v0
	v_lshl_add_u64 v[0:1], v[0:1], 1, v[86:87]
	global_load_dwordx2 v[30:31], v[0:1], off
	s_waitcnt vmcnt(0)
	v_cvt_f32_f16_e32 v32, v30
	v_cvt_f32_f16_sdwa v33, v30 dst_sel:DWORD dst_unused:UNUSED_PAD src0_sel:WORD_1
	v_cvt_f32_f16_e32 v30, v31
	v_cvt_f32_f16_sdwa v31, v31 dst_sel:DWORD dst_unused:UNUSED_PAD src0_sel:WORD_1
	v_pk_add_f32 v[26:27], v[26:27], v[32:33]
	s_nop 0
	v_cvt_pk_f16_f32 v26, v26, v27
	v_pk_add_f32 v[28:29], v[28:29], v[30:31]
	s_nop 0
	v_cvt_pk_f16_f32 v27, v28, v29
	global_store_dwordx2 v[0:1], v[26:27], off
.LBB5_9:
	s_or_b64 exec, exec, s[0:1]
	s_and_saveexec_b64 s[0:1], s[4:5]
	s_cbranch_execz .LBB5_12
	s_nop 2
	ds_read_b128 v[26:29], v96
	s_waitcnt vmcnt(2)
	ds_read_b128 v[30:33], v96 offset:512
	v_cvt_f32_f16_sdwa v55, v42 dst_sel:DWORD dst_unused:UNUSED_PAD src0_sel:WORD_1
	v_cvt_f32_f16_e32 v54, v42
	s_waitcnt vmcnt(1)
	v_lshlrev_b32_e32 v50, 4, v97
	v_or_b32_e32 v0, v50, v94
	s_waitcnt lgkmcnt(0)
	v_fma_mix_f32 v26, v26, v38, v30 op_sel_hi:[0,1,0]
	v_fma_mix_f32 v27, v27, v38, v31 op_sel:[0,1,0] op_sel_hi:[0,1,0]
	v_ashrrev_i32_e32 v1, 31, v0
	v_max_f32_e32 v26, 0, v26
	v_max_f32_e32 v27, 0, v27
	s_waitcnt vmcnt(0)
	v_lshlrev_b64 v[34:35], 8, v[0:1]
	v_pk_add_f32 v[30:31], v[26:27], v[54:55]
	v_cvt_f32_f16_sdwa v27, v43 dst_sel:DWORD dst_unused:UNUSED_PAD src0_sel:WORD_1
	v_cvt_f32_f16_e32 v26, v43
	v_lshl_add_u64 v[52:53], v[82:83], 0, v[34:35]
	ds_read_b128 v[34:37], v96 offset:16
	ds_read_b128 v[46:49], v96 offset:528
	v_fma_mix_f32 v28, v28, v39, v32 op_sel_hi:[0,1,0]
	v_fma_mix_f32 v29, v29, v39, v33 op_sel:[0,1,0] op_sel_hi:[0,1,0]
	v_max_f32_e32 v28, 0, v28
	v_max_f32_e32 v29, 0, v29
	v_pk_add_f32 v[28:29], v[28:29], v[26:27]
	v_cvt_f32_f16_sdwa v27, v44 dst_sel:DWORD dst_unused:UNUSED_PAD src0_sel:WORD_1
	v_cvt_f32_f16_e32 v26, v44
	s_waitcnt lgkmcnt(0)
	v_fma_mix_f32 v32, v34, v40, v46 op_sel_hi:[0,1,0]
	v_fma_mix_f32 v33, v35, v40, v47 op_sel:[0,1,0] op_sel_hi:[0,1,0]
	v_max_f32_e32 v32, 0, v32
	v_max_f32_e32 v33, 0, v33
	v_pk_add_f32 v[32:33], v[32:33], v[26:27]
	v_cvt_f32_f16_sdwa v27, v45 dst_sel:DWORD dst_unused:UNUSED_PAD src0_sel:WORD_1
	v_cvt_f32_f16_e32 v26, v45
	v_fma_mix_f32 v34, v36, v41, v48 op_sel_hi:[0,1,0]
	v_fma_mix_f32 v35, v37, v41, v49 op_sel:[0,1,0] op_sel_hi:[0,1,0]
	v_max_f32_e32 v34, 0, v34
	v_max_f32_e32 v35, 0, v35
	v_pk_add_f32 v[34:35], v[34:35], v[26:27]
	v_mov_b32_e32 v26, 0
	v_cvt_pk_fp8_f32 v26, v30, v31
	v_cvt_pk_f16_f32 v38, v30, v31
	v_cvt_pk_f16_f32 v39, v28, v29
	v_cvt_pk_f16_f32 v40, v32, v33
	v_cvt_pk_f16_f32 v41, v34, v35
	global_store_dwordx4 v[52:53], v[38:41], off
	v_cvt_pk_fp8_f32 v26, v28, v29 op_sel:[0,0,1]
	ds_read_b128 v[28:31], v96 offset:128
	ds_read_b128 v[42:45], v96 offset:640
	v_mov_b32_e32 v27, 0
	v_cvt_f32_f16_sdwa v55, v22 dst_sel:DWORD dst_unused:UNUSED_PAD src0_sel:WORD_1
	v_cvt_f32_f16_e32 v54, v22
	v_cvt_pk_fp8_f32 v27, v32, v33
	s_waitcnt lgkmcnt(0)
	v_fma_mix_f32 v28, v28, v18, v42 op_sel_hi:[0,1,0]
	v_fma_mix_f32 v18, v29, v18, v43 op_sel:[0,1,0] op_sel_hi:[0,1,0]
	v_max_f32_e32 v28, 0, v28
	v_max_f32_e32 v29, 0, v18
	v_pk_add_f32 v[42:43], v[28:29], v[54:55]
	v_cvt_f32_f16_sdwa v29, v23 dst_sel:DWORD dst_unused:UNUSED_PAD src0_sel:WORD_1
	v_cvt_f32_f16_e32 v28, v23
	v_cvt_pk_fp8_f32 v27, v34, v35 op_sel:[0,0,1]
	ds_bpermute_b32 v34, v95, v38
	ds_bpermute_b32 v35, v95, v39
	ds_bpermute_b32 v36, v95, v40
	ds_bpermute_b32 v37, v95, v41
	ds_read_b128 v[38:41], v96 offset:144
	ds_read_b128 v[46:49], v96 offset:656
	v_fma_mix_f32 v22, v30, v19, v44 op_sel_hi:[0,1,0]
	v_fma_mix_f32 v19, v31, v19, v45 op_sel:[0,1,0] op_sel_hi:[0,1,0]
	v_max_f32_e32 v22, 0, v22
	v_max_f32_e32 v23, 0, v19
	v_pk_add_f32 v[22:23], v[22:23], v[28:29]
	v_cvt_f32_f16_sdwa v29, v24 dst_sel:DWORD dst_unused:UNUSED_PAD src0_sel:WORD_1
	v_cvt_f32_f16_e32 v28, v24
	s_waitcnt lgkmcnt(0)
	v_fma_mix_f32 v30, v38, v20, v46 op_sel_hi:[0,1,0]
	v_fma_mix_f32 v20, v39, v20, v47 op_sel:[0,1,0] op_sel_hi:[0,1,0]
	v_fma_mix_f32 v24, v40, v21, v48 op_sel_hi:[0,1,0]
	v_fma_mix_f32 v21, v41, v21, v49 op_sel:[0,1,0] op_sel_hi:[0,1,0]
	v_cvt_f32_f16_sdwa v41, v25 dst_sel:DWORD dst_unused:UNUSED_PAD src0_sel:WORD_1
	v_cvt_f32_f16_e32 v40, v25
	v_max_f32_e32 v30, 0, v30
	v_max_f32_e32 v31, 0, v20
	v_pk_add_f32 v[30:31], v[30:31], v[28:29]
	v_mov_b32_e32 v28, 0
	v_mov_b32_e32 v29, 0
	v_max_f32_e32 v38, 0, v24
	v_max_f32_e32 v39, 0, v21
	v_cvt_pk_fp8_f32 v28, v42, v43
	v_cvt_pk_fp8_f32 v29, v30, v31
	v_pk_add_f32 v[24:25], v[38:39], v[40:41]
	v_cvt_pk_f16_f32 v18, v42, v43
	v_cvt_pk_f16_f32 v19, v22, v23
	v_cvt_pk_f16_f32 v20, v30, v31
	v_cvt_pk_f16_f32 v21, v24, v25
	global_store_dwordx4 v[52:53], v[18:21], off offset:64
	v_cvt_pk_fp8_f32 v28, v22, v23 op_sel:[0,0,1]
	v_cvt_pk_fp8_f32 v29, v24, v25 op_sel:[0,0,1]
	ds_read_b128 v[22:25], v96 offset:256
	ds_read_b128 v[38:41], v96 offset:768
	ds_read_b128 v[42:45], v96 offset:272
	ds_read_b128 v[46:49], v96 offset:784
	v_cvt_f32_f16_sdwa v31, v14 dst_sel:DWORD dst_unused:UNUSED_PAD src0_sel:WORD_1
	s_waitcnt lgkmcnt(2)
	v_fma_mix_f32 v22, v22, v10, v38 op_sel_hi:[0,1,0]
	v_cvt_f32_f16_e32 v30, v14
	v_fma_mix_f32 v10, v23, v10, v39 op_sel:[0,1,0] op_sel_hi:[0,1,0]
	v_fma_mix_f32 v14, v24, v11, v40 op_sel_hi:[0,1,0]
	v_fma_mix_f32 v11, v25, v11, v41 op_sel:[0,1,0] op_sel_hi:[0,1,0]
	v_max_f32_e32 v22, 0, v22
	v_max_f32_e32 v23, 0, v10
	v_pk_add_f32 v[22:23], v[22:23], v[30:31]
	v_cvt_f32_f16_sdwa v31, v15 dst_sel:DWORD dst_unused:UNUSED_PAD src0_sel:WORD_1
	v_cvt_f32_f16_e32 v30, v15
	v_cvt_f32_f16_sdwa v25, v16 dst_sel:DWORD dst_unused:UNUSED_PAD src0_sel:WORD_1
	v_cvt_f32_f16_e32 v24, v16
	v_max_f32_e32 v14, 0, v14
	v_max_f32_e32 v15, 0, v11
	v_pk_add_f32 v[14:15], v[14:15], v[30:31]
	s_waitcnt lgkmcnt(0)
	v_fma_mix_f32 v30, v42, v12, v46 op_sel_hi:[0,1,0]
	v_fma_mix_f32 v12, v43, v12, v47 op_sel:[0,1,0] op_sel_hi:[0,1,0]
	v_fma_mix_f32 v16, v44, v13, v48 op_sel_hi:[0,1,0]
	v_fma_mix_f32 v13, v45, v13, v49 op_sel:[0,1,0] op_sel_hi:[0,1,0]
	v_cvt_f32_f16_sdwa v45, v17 dst_sel:DWORD dst_unused:UNUSED_PAD src0_sel:WORD_1
	v_cvt_f32_f16_e32 v44, v17
	v_max_f32_e32 v30, 0, v30
	v_max_f32_e32 v31, 0, v12
	v_pk_add_f32 v[24:25], v[30:31], v[24:25]
	v_mov_b32_e32 v30, 0
	v_mov_b32_e32 v31, 0
	v_max_f32_e32 v42, 0, v16
	v_max_f32_e32 v43, 0, v13
	v_cvt_pk_fp8_f32 v30, v22, v23
	v_cvt_pk_fp8_f32 v31, v24, v25
	v_pk_add_f32 v[16:17], v[42:43], v[44:45]
	v_cvt_pk_f16_f32 v10, v22, v23
	v_cvt_pk_f16_f32 v11, v14, v15
	v_cvt_pk_f16_f32 v12, v24, v25
	v_cvt_pk_f16_f32 v13, v16, v17
	global_store_dwordx4 v[52:53], v[10:13], off offset:128
	v_cvt_pk_fp8_f32 v30, v14, v15 op_sel:[0,0,1]
	v_cvt_pk_fp8_f32 v31, v16, v17 op_sel:[0,0,1]
	ds_read_b128 v[14:17], v96 offset:384
	ds_read_b128 v[22:25], v96 offset:896
	ds_read_b128 v[42:45], v96 offset:400
	ds_read_b128 v[46:49], v96 offset:912
	v_cvt_f32_f16_sdwa v67, v6 dst_sel:DWORD dst_unused:UNUSED_PAD src0_sel:WORD_1
	v_cvt_f32_f16_e32 v66, v6
	ds_bpermute_b32 v18, v95, v18
	s_waitcnt lgkmcnt(3)
	v_fma_mix_f32 v14, v14, v2, v22 op_sel_hi:[0,1,0]
	v_fma_mix_f32 v2, v15, v2, v23 op_sel:[0,1,0] op_sel_hi:[0,1,0]
	v_cvt_f32_f16_sdwa v23, v7 dst_sel:DWORD dst_unused:UNUSED_PAD src0_sel:WORD_1
	v_cvt_f32_f16_e32 v22, v7
	v_fma_mix_f32 v6, v16, v3, v24 op_sel_hi:[0,1,0]
	v_fma_mix_f32 v3, v17, v3, v25 op_sel:[0,1,0] op_sel_hi:[0,1,0]
	v_cvt_f32_f16_sdwa v17, v8 dst_sel:DWORD dst_unused:UNUSED_PAD src0_sel:WORD_1
	v_cvt_f32_f16_e32 v16, v8
	v_max_f32_e32 v6, 0, v6
	v_max_f32_e32 v7, 0, v3
	ds_bpermute_b32 v19, v95, v19
	ds_bpermute_b32 v20, v95, v20
	ds_bpermute_b32 v21, v95, v21
	v_pk_add_f32 v[6:7], v[6:7], v[22:23]
	s_waitcnt lgkmcnt(4)
	v_fma_mix_f32 v22, v42, v4, v46 op_sel_hi:[0,1,0]
	v_fma_mix_f32 v4, v43, v4, v47 op_sel:[0,1,0] op_sel_hi:[0,1,0]
	v_max_f32_e32 v22, 0, v22
	v_max_f32_e32 v23, 0, v4
	v_max_f32_e32 v14, 0, v14
	v_max_f32_e32 v15, 0, v2
	v_pk_add_f32 v[16:17], v[22:23], v[16:17]
	v_cvt_f32_f16_sdwa v23, v9 dst_sel:DWORD dst_unused:UNUSED_PAD src0_sel:WORD_1
	v_cvt_f32_f16_e32 v22, v9
	v_pk_add_f32 v[14:15], v[14:15], v[66:67]
	v_mov_b32_e32 v32, 0
	v_mov_b32_e32 v33, 0
	ds_bpermute_b32 v10, v95, v10
	ds_bpermute_b32 v11, v95, v11
	ds_bpermute_b32 v12, v95, v12
	ds_bpermute_b32 v13, v95, v13
	v_fma_mix_f32 v8, v44, v5, v48 op_sel_hi:[0,1,0]
	v_fma_mix_f32 v5, v45, v5, v49 op_sel:[0,1,0] op_sel_hi:[0,1,0]
	v_cvt_pk_fp8_f32 v32, v14, v15
	v_cvt_pk_f16_f32 v2, v14, v15
	v_cvt_pk_f16_f32 v4, v16, v17
	v_max_f32_e32 v8, 0, v8
	v_max_f32_e32 v9, 0, v5
	v_cvt_pk_fp8_f32 v33, v16, v17
	s_nop 0
	v_mfma_f32_16x16x32_f16 v[14:17], v[34:37], v[112:115], 0
	v_add_f32_e64 v22, v8, v22
	v_add_f32_e64 v23, v9, v23
	v_cvt_pk_f16_f32 v3, v6, v7
	v_cvt_pk_f16_f32 v5, v22, v23
	v_cvt_pk_fp8_f32 v32, v6, v7 op_sel:[0,0,1]
	ds_bpermute_b32 v6, v95, v2
	ds_bpermute_b32 v7, v95, v3
	ds_bpermute_b32 v8, v95, v4
	ds_bpermute_b32 v9, v95, v5
	s_waitcnt lgkmcnt(8)
	v_mfma_f32_16x16x32_f16 v[14:17], v[18:21], v[116:119], v[14:17]
	global_store_dwordx4 v[52:53], v[2:5], off offset:192
	v_cvt_pk_fp8_f32 v33, v22, v23 op_sel:[0,0,1]
	s_nop 0
	v_lshlrev_b64 v[4:5], 7, v[0:1]
	s_waitcnt lgkmcnt(4)
	v_mfma_f32_16x16x32_f16 v[0:3], v[10:13], v[120:123], v[14:17]
	v_lshl_add_u64 v[4:5], v[84:85], 0, v[4:5]
	global_store_dwordx4 v[4:5], v[26:29], off
	global_store_dwordx4 v[4:5], v[30:33], off offset:64
	s_waitcnt lgkmcnt(0)
	v_mfma_f32_16x16x32_f16 v[0:3], v[6:9], v[124:127], v[0:3]
	s_and_b64 exec, exec, vcc
	s_cbranch_execz .LBB5_12
	v_mul_u32_u24_e32 v50, 10, v50
	v_ashrrev_i32_e32 v51, 31, v50
	v_lshl_add_u64 v[4:5], v[50:51], 1, v[86:87]
	global_load_dwordx2 v[6:7], v[4:5], off
	s_waitcnt vmcnt(0)
	v_cvt_f32_f16_e32 v8, v6
	v_cvt_f32_f16_sdwa v9, v6 dst_sel:DWORD dst_unused:UNUSED_PAD src0_sel:WORD_1
	v_cvt_f32_f16_e32 v6, v7
	v_cvt_f32_f16_sdwa v7, v7 dst_sel:DWORD dst_unused:UNUSED_PAD src0_sel:WORD_1
	v_pk_add_f32 v[0:1], v[0:1], v[8:9]
	s_nop 0
	v_cvt_pk_f16_f32 v0, v0, v1
	v_pk_add_f32 v[2:3], v[2:3], v[6:7]
	s_nop 0
	v_cvt_pk_f16_f32 v1, v2, v3
	global_store_dwordx2 v[4:5], v[0:1], off

	.amdhsa_kernel _Z8k_updateILi1EEvPKDF16_PKfS3_S3_PDF16_PhPKDv8_DF16_PKiPfSB_
		.amdhsa_group_segment_fixed_size 1024
		.amdhsa_private_segment_fixed_size 0
		.amdhsa_kernarg_size 80
		.amdhsa_user_sgpr_count 2
		.amdhsa_user_sgpr_dispatch_ptr 0
		.amdhsa_user_sgpr_queue_ptr 0
		.amdhsa_user_sgpr_kernarg_segment_ptr 1
		.amdhsa_user_sgpr_dispatch_id 0
		.amdhsa_user_sgpr_kernarg_preload_length 0
		.amdhsa_user_sgpr_kernarg_preload_offset 0
		.amdhsa_user_sgpr_private_segment_size 0
		.amdhsa_uses_dynamic_stack 0
		.amdhsa_enable_private_segment 0
		.amdhsa_system_sgpr_workgroup_id_x 1
		.amdhsa_system_sgpr_workgroup_id_y 0
		.amdhsa_system_sgpr_workgroup_id_z 0
		.amdhsa_system_sgpr_workgroup_info 0
		.amdhsa_system_vgpr_workitem_id 0
		.amdhsa_next_free_vgpr 128
		.amdhsa_next_free_sgpr 22
		.amdhsa_accum_offset 128
		.amdhsa_reserve_vcc 1
		.amdhsa_float_round_mode_32 0
		.amdhsa_float_round_mode_16_64 0
		.amdhsa_float_denorm_mode_32 3
		.amdhsa_float_denorm_mode_16_64 3
		.amdhsa_dx10_clamp 1
		.amdhsa_ieee_mode 1
		.amdhsa_fp16_overflow 0
		.amdhsa_tg_split 0
		.amdhsa_exception_fp_ieee_invalid_op 0
		.amdhsa_exception_fp_denorm_src 0
		.amdhsa_exception_fp_ieee_div_zero 0
		.amdhsa_exception_fp_ieee_overflow 0
		.amdhsa_exception_fp_ieee_underflow 0
		.amdhsa_exception_fp_ieee_inexact 0
		.amdhsa_exception_int_div_zero 0
	.end_amdhsa_kernel

amdhsa.kernels:
  - .agpr_count:     0
    .args:
      - .actual_access:  read_only
        .address_space:  global
        .offset:         0
        .size:           8
        .value_kind:     global_buffer
      - .actual_access:  read_only
        .address_space:  global
        .offset:         8
        .size:           8
        .value_kind:     global_buffer
      - .actual_access:  write_only
        .address_space:  global
        .offset:         16
        .size:           8
        .value_kind:     global_buffer
      - .actual_access:  write_only
        .address_space:  global
        .offset:         24
        .size:           8
        .value_kind:     global_buffer
      - .actual_access:  read_only
        .address_space:  global
        .offset:         32
        .size:           8
        .value_kind:     global_buffer
      - .actual_access:  read_only
        .address_space:  global
        .offset:         40
        .size:           8
        .value_kind:     global_buffer
      - .actual_access:  read_only
        .address_space:  global
        .offset:         48
        .size:           8
        .value_kind:     global_buffer
      - .actual_access:  read_only
        .address_space:  global
        .offset:         56
        .size:           8
        .value_kind:     global_buffer
      - .actual_access:  read_only
        .address_space:  global
        .offset:         64
        .size:           8
        .value_kind:     global_buffer
      - .actual_access:  read_only
        .address_space:  global
        .offset:         72
        .size:           8
        .value_kind:     global_buffer
      - .actual_access:  read_only
        .address_space:  global
        .offset:         80
        .size:           8
        .value_kind:     global_buffer
      - .actual_access:  write_only
        .address_space:  global
        .offset:         88
        .size:           8
        .value_kind:     global_buffer
      - .actual_access:  write_only
        .address_space:  global
        .offset:         96
        .size:           8
        .value_kind:     global_buffer
      - .actual_access:  write_only
        .address_space:  global
        .offset:         104
        .size:           8
        .value_kind:     global_buffer
      - .offset:         112
        .size:           4
        .value_kind:     by_value
      - .actual_access:  write_only
        .address_space:  global
        .offset:         120
        .size:           8
        .value_kind:     global_buffer
      - .offset:         128
        .size:           4
        .value_kind:     by_value
    .group_segment_fixed_size: 38944
    .kernarg_segment_align: 8
    .kernarg_segment_size: 132
    .language:       OpenCL C
    .language_version:
      - 2
      - 0
    .max_flat_workgroup_size: 512
    .name:           _Z6k_pre1PK15HIP_vector_typeIiLj4EES2_PiPjPKfS6_S6_S6_S6_S6_S6_PDF16_S7_S3_iS3_i
    .private_segment_fixed_size: 0
    .sgpr_count:     28
    .sgpr_spill_count: 0
    .symbol:         _Z6k_pre1PK15HIP_vector_typeIiLj4EES2_PiPjPKfS6_S6_S6_S6_S6_S6_PDF16_S7_S3_iS3_i.kd
    .uniform_work_group_size: 1
    .uses_dynamic_stack: false
    .vgpr_count:     61
    .vgpr_spill_count: 0
    .wavefront_size: 64
  - .agpr_count:     0
    .args:
      - .actual_access:  read_only
        .address_space:  global
        .offset:         0
        .size:           8
        .value_kind:     global_buffer
      - .actual_access:  read_only
        .address_space:  global
        .offset:         8
        .size:           8
        .value_kind:     global_buffer
      - .actual_access:  write_only
        .address_space:  global
        .offset:         16
        .size:           8
        .value_kind:     global_buffer
      - .actual_access:  write_only
        .address_space:  global
        .offset:         24
        .size:           8
        .value_kind:     global_buffer
      - .actual_access:  read_only
        .address_space:  global
        .offset:         32
        .size:           8
        .value_kind:     global_buffer
      - .actual_access:  read_only
        .address_space:  global
        .offset:         40
        .size:           8
        .value_kind:     global_buffer
      - .actual_access:  read_only
        .address_space:  global
        .offset:         48
        .size:           8
        .value_kind:     global_buffer
      - .actual_access:  read_only
        .address_space:  global
        .offset:         56
        .size:           8
        .value_kind:     global_buffer
      - .actual_access:  read_only
        .address_space:  global
        .offset:         64
        .size:           8
        .value_kind:     global_buffer
      - .actual_access:  write_only
        .address_space:  global
        .offset:         72
        .size:           8
        .value_kind:     global_buffer
      - .actual_access:  write_only
        .address_space:  global
        .offset:         80
        .size:           8
        .value_kind:     global_buffer
      - .actual_access:  write_only
        .address_space:  global
        .offset:         88
        .size:           8
        .value_kind:     global_buffer
      - .offset:         96
        .size:           4
        .value_kind:     hidden_block_count_x
      - .offset:         100
        .size:           4
        .value_kind:     hidden_block_count_y
      - .offset:         104
        .size:           4
        .value_kind:     hidden_block_count_z
      - .offset:         108
        .size:           2
        .value_kind:     hidden_group_size_x
      - .offset:         110
        .size:           2
        .value_kind:     hidden_group_size_y
      - .offset:         112
        .size:           2
        .value_kind:     hidden_group_size_z
      - .offset:         114
        .size:           2
        .value_kind:     hidden_remainder_x
      - .offset:         116
        .size:           2
        .value_kind:     hidden_remainder_y
      - .offset:         118
        .size:           2
        .value_kind:     hidden_remainder_z
      - .offset:         136
        .size:           8
        .value_kind:     hidden_global_offset_x
      - .offset:         144
        .size:           8
        .value_kind:     hidden_global_offset_y
      - .offset:         152
        .size:           8
        .value_kind:     hidden_global_offset_z
      - .offset:         160
        .size:           2
        .value_kind:     hidden_grid_dims
    .group_segment_fixed_size: 63520
    .kernarg_segment_align: 8
    .kernarg_segment_size: 352
    .language:       OpenCL C
    .language_version:
      - 2
      - 0
    .max_flat_workgroup_size: 512
    .name:           _Z6k_pre2PKjPKiPiS3_PKfPKDv8_DF16_S5_S8_S2_PDF16_PhPf
    .private_segment_fixed_size: 0
    .sgpr_count:     36
    .sgpr_spill_count: 0
    .symbol:         _Z6k_pre2PKjPKiPiS3_PKfPKDv8_DF16_S5_S8_S2_PDF16_PhPf.kd
    .uniform_work_group_size: 1
    .uses_dynamic_stack: false
    .vgpr_count:     107
    .vgpr_spill_count: 0
    .wavefront_size: 64
  - .agpr_count:     0
    .args:
      - .actual_access:  read_only
        .address_space:  global
        .offset:         0
        .size:           8
        .value_kind:     global_buffer
      - .actual_access:  read_only
        .address_space:  global
        .offset:         8
        .size:           8
        .value_kind:     global_buffer
      - .actual_access:  read_only
        .address_space:  global
        .offset:         16
        .size:           8
        .value_kind:     global_buffer
      - .actual_access:  read_only
        .address_space:  global
        .offset:         24
        .size:           8
        .value_kind:     global_buffer
      - .actual_access:  read_only
        .address_space:  global
        .offset:         32
        .size:           8
        .value_kind:     global_buffer
      - .actual_access:  read_only
        .address_space:  global
        .offset:         40
        .size:           8
        .value_kind:     global_buffer
      - .actual_access:  write_only
        .address_space:  global
        .offset:         48
        .size:           8
        .value_kind:     global_buffer
      - .address_space:  global
        .offset:         56
        .size:           8
        .value_kind:     global_buffer
      - .offset:         64
        .size:           4
        .value_kind:     hidden_block_count_x
      - .offset:         68
        .size:           4
        .value_kind:     hidden_block_count_y
      - .offset:         72
        .size:           4
        .value_kind:     hidden_block_count_z
      - .offset:         76
        .size:           2
        .value_kind:     hidden_group_size_x
      - .offset:         78
        .size:           2
        .value_kind:     hidden_group_size_y
      - .offset:         80
        .size:           2
        .value_kind:     hidden_group_size_z
      - .offset:         82
        .size:           2
        .value_kind:     hidden_remainder_x
      - .offset:         84
        .size:           2
        .value_kind:     hidden_remainder_y
      - .offset:         86
        .size:           2
        .value_kind:     hidden_remainder_z
      - .offset:         104
        .size:           8
        .value_kind:     hidden_global_offset_x
      - .offset:         112
        .size:           8
        .value_kind:     hidden_global_offset_y
      - .offset:         120
        .size:           8
        .value_kind:     hidden_global_offset_z
      - .offset:         128
        .size:           2
        .value_kind:     hidden_grid_dims
    .group_segment_fixed_size: 36864
    .kernarg_segment_align: 8
    .kernarg_segment_size: 320
    .language:       OpenCL C
    .language_version:
      - 2
      - 0
    .max_flat_workgroup_size: 256
    .name:           _Z5k_aggPKDF16_PKhPKiS4_PKDv8_DF16_PKfPDF16_Pf
    .private_segment_fixed_size: 0
    .sgpr_count:     25
    .sgpr_spill_count: 0
    .symbol:         _Z5k_aggPKDF16_PKhPKiS4_PKDv8_DF16_PKfPDF16_Pf.kd
    .uniform_work_group_size: 1
    .uses_dynamic_stack: false
    .vgpr_count:     108
    .vgpr_spill_count: 0
    .wavefront_size: 64
  - .agpr_count:     0
    .args:
      - .actual_access:  read_only
        .address_space:  global
        .offset:         0
        .size:           8
        .value_kind:     global_buffer
      - .actual_access:  read_only
        .address_space:  global
        .offset:         8
        .size:           8
        .value_kind:     global_buffer
      - .actual_access:  write_only
        .address_space:  global
        .offset:         16
        .size:           8
        .value_kind:     global_buffer
      - .offset:         24
        .size:           4
        .value_kind:     hidden_block_count_x
      - .offset:         28
        .size:           4
        .value_kind:     hidden_block_count_y
      - .offset:         32
        .size:           4
        .value_kind:     hidden_block_count_z
      - .offset:         36
        .size:           2
        .value_kind:     hidden_group_size_x
      - .offset:         38
        .size:           2
        .value_kind:     hidden_group_size_y
      - .offset:         40
        .size:           2
        .value_kind:     hidden_group_size_z
      - .offset:         42
        .size:           2
        .value_kind:     hidden_remainder_x
      - .offset:         44
        .size:           2
        .value_kind:     hidden_remainder_y
      - .offset:         46
        .size:           2
        .value_kind:     hidden_remainder_z
      - .offset:         64
        .size:           8
        .value_kind:     hidden_global_offset_x
      - .offset:         72
        .size:           8
        .value_kind:     hidden_global_offset_y
      - .offset:         80
        .size:           8
        .value_kind:     hidden_global_offset_z
      - .offset:         88
        .size:           2
        .value_kind:     hidden_grid_dims
    .group_segment_fixed_size: 0
    .kernarg_segment_align: 8
    .kernarg_segment_size: 280
    .language:       OpenCL C
    .language_version:
      - 2
      - 0
    .max_flat_workgroup_size: 1024
    .name:           _Z5k_outPKiPKfPf
    .private_segment_fixed_size: 0
    .sgpr_count:     14
    .sgpr_spill_count: 0
    .symbol:         _Z5k_outPKiPKfPf.kd
    .uniform_work_group_size: 1
    .uses_dynamic_stack: false
    .vgpr_count:     44
    .vgpr_spill_count: 0
    .wavefront_size: 64
  - .agpr_count:     0
    .args:
      - .address_space:  global
        .offset:         0
        .size:           8
        .value_kind:     global_buffer
      - .actual_access:  read_only
        .address_space:  global
        .offset:         8
        .size:           8
        .value_kind:     global_buffer
      - .actual_access:  read_only
        .address_space:  global
        .offset:         16
        .size:           8
        .value_kind:     global_buffer
      - .actual_access:  read_only
        .address_space:  global
        .offset:         24
        .size:           8
        .value_kind:     global_buffer
      - .actual_access:  read_only
        .address_space:  global
        .offset:         32
        .size:           8
        .value_kind:     global_buffer
      - .actual_access:  read_only
        .address_space:  global
        .offset:         40
        .size:           8
        .value_kind:     global_buffer
      - .actual_access:  read_only
        .address_space:  global
        .offset:         48
        .size:           8
        .value_kind:     global_buffer
      - .address_space:  global
        .offset:         56
        .size:           8
        .value_kind:     global_buffer
      - .offset:         64
        .size:           4
        .value_kind:     hidden_block_count_x
      - .offset:         68
        .size:           4
        .value_kind:     hidden_block_count_y
      - .offset:         72
        .size:           4
        .value_kind:     hidden_block_count_z
      - .offset:         76
        .size:           2
        .value_kind:     hidden_group_size_x
      - .offset:         78
        .size:           2
        .value_kind:     hidden_group_size_y
      - .offset:         80
        .size:           2
        .value_kind:     hidden_group_size_z
      - .offset:         82
        .size:           2
        .value_kind:     hidden_remainder_x
      - .offset:         84
        .size:           2
        .value_kind:     hidden_remainder_y
      - .offset:         86
        .size:           2
        .value_kind:     hidden_remainder_z
      - .offset:         104
        .size:           8
        .value_kind:     hidden_global_offset_x
      - .offset:         112
        .size:           8
        .value_kind:     hidden_global_offset_y
      - .offset:         120
        .size:           8
        .value_kind:     hidden_global_offset_z
      - .offset:         128
        .size:           2
        .value_kind:     hidden_grid_dims
    .group_segment_fixed_size: 41984
    .kernarg_segment_align: 8
    .kernarg_segment_size: 320
    .language:       OpenCL C
    .language_version:
      - 2
      - 0
    .max_flat_workgroup_size: 512
    .name:           _Z6k_mlp2ILi0EEvPDF16_PKfS2_S2_PKDv8_DF16_S2_S2_Pf
    .private_segment_fixed_size: 0
    .sgpr_count:     29
    .sgpr_spill_count: 0
    .symbol:         _Z6k_mlp2ILi0EEvPDF16_PKfS2_S2_PKDv8_DF16_S2_S2_Pf.kd
    .uniform_work_group_size: 1
    .uses_dynamic_stack: false
    .vgpr_count:     76
    .vgpr_spill_count: 0
    .wavefront_size: 64
  - .agpr_count:     0
    .args:
      - .actual_access:  read_only
        .address_space:  global
        .offset:         0
        .size:           8
        .value_kind:     global_buffer
      - .actual_access:  read_only
        .address_space:  global
        .offset:         8
        .size:           8
        .value_kind:     global_buffer
      - .actual_access:  read_only
        .address_space:  global
        .offset:         16
        .size:           8
        .value_kind:     global_buffer
      - .actual_access:  read_only
        .address_space:  global
        .offset:         24
        .size:           8
        .value_kind:     global_buffer
      - .address_space:  global
        .offset:         32
        .size:           8
        .value_kind:     global_buffer
      - .actual_access:  write_only
        .address_space:  global
        .offset:         40
        .size:           8
        .value_kind:     global_buffer
      - .actual_access:  read_only
        .address_space:  global
        .offset:         48
        .size:           8
        .value_kind:     global_buffer
      - .actual_access:  read_only
        .address_space:  global
        .offset:         56
        .size:           8
        .value_kind:     global_buffer
      - .actual_access:  read_only
        .address_space:  global
        .offset:         64
        .size:           8
        .value_kind:     global_buffer
      - .address_space:  global
        .offset:         72
        .size:           8
        .value_kind:     global_buffer
    .group_segment_fixed_size: 1024
    .kernarg_segment_align: 8
    .kernarg_segment_size: 80
    .language:       OpenCL C
    .language_version:
      - 2
      - 0
    .max_flat_workgroup_size: 512
    .name:           _Z8k_updateILi1EEvPKDF16_PKfS3_S3_PDF16_PhPKDv8_DF16_PKiPfSB_
    .private_segment_fixed_size: 0
    .sgpr_count:     25
    .sgpr_spill_count: 0
    .symbol:         _Z8k_updateILi1EEvPKDF16_PKfS3_S3_PDF16_PhPKDv8_DF16_PKiPfSB_.kd
    .uniform_work_group_size: 1
    .uses_dynamic_stack: false
    .vgpr_count:     128
    .vgpr_spill_count: 0
    .wavefront_size: 64
  - .agpr_count:     0
    .args:
      - .actual_access:  read_only
        .address_space:  global
        .offset:         0
        .size:           8
        .value_kind:     global_buffer
      - .actual_access:  read_only
        .address_space:  global
        .offset:         8
        .size:           8
        .value_kind:     global_buffer
      - .actual_access:  read_only
        .address_space:  global
        .offset:         16
        .size:           8
        .value_kind:     global_buffer
      - .actual_access:  read_only
        .address_space:  global
        .offset:         24
        .size:           8
        .value_kind:     global_buffer
      - .actual_access:  read_only
        .address_space:  global
        .offset:         32
        .size:           8
        .value_kind:     global_buffer
      - .actual_access:  read_only
        .address_space:  global
        .offset:         40
        .size:           8
        .value_kind:     global_buffer
      - .actual_access:  read_only
        .address_space:  global
        .offset:         48
        .size:           8
        .value_kind:     global_buffer
      - .actual_access:  read_only
        .address_space:  global
        .offset:         56
        .size:           8
        .value_kind:     global_buffer
      - .address_space:  global
        .offset:         64
        .size:           8
        .value_kind:     global_buffer
      - .actual_access:  read_only
        .address_space:  global
        .offset:         72
        .size:           8
        .value_kind:     global_buffer
    .group_segment_fixed_size: 6656
    .kernarg_segment_align: 8
    .kernarg_segment_size: 80
    .language:       OpenCL C
    .language_version:
      - 2
      - 0
    .max_flat_workgroup_size: 512
    .name:           _Z8k_updateILi2EEvPKDF16_PKfS3_S3_PDF16_PhPKDv8_DF16_PKiPfSB_
    .private_segment_fixed_size: 0
    .sgpr_count:     36
    .sgpr_spill_count: 0
    .symbol:         _Z8k_updateILi2EEvPKDF16_PKfS3_S3_PDF16_PhPKDv8_DF16_PKiPfSB_.kd
    .uniform_work_group_size: 1
    .uses_dynamic_stack: false
    .vgpr_count:     104
    .vgpr_spill_count: 0
    .wavefront_size: 64
